# barrier after in-projection split: arrive only; attention setup and copy-first waves go on, each wave waits for completion before its first attention unit
# speedup vs baseline: 1.0044x; 1.0044x over previous
; __device__ __forceinline__ unsigned xb_ld(unsigned* p)              { return __hip_atomic_load(p, __ATOMIC_RELAXED, __HIP_MEMORY_SCOPE_AGENT); }
; __device__ __forceinline__ unsigned xb_add(unsigned* p, unsigned v) { return __hip_atomic_fetch_add(p, v, __ATOMIC_RELAXED, __HIP_MEMORY_SCOPE_AGENT); }
; #define XB_SPIN(cond, bar) do { unsigned _sp = 0; while (cond) { __builtin_amdgcn_s_sleep(1); \
;     if ((++_sp & 255u) == 0u) { if (xb_ld(&(bar)[XB_TMO])) break; if (_sp > XB_SPIN_CAP) { atomicAdd(&(bar)[XB_TMO], 1u); break; } } } } while (0)
; __device__ __forceinline__ void xcd_barrier(const XcdBarrier& b, const int tid) {
;     ...
;         const unsigned old = xb_add(&bar[XB_XSUB(b.x)], 1u);
;         const unsigned gen = old / nloc;
;         if (old + 1u == (gen + 1u) * nloc) {
;             __builtin_amdgcn_fence(__ATOMIC_RELEASE, "agent");
;             asm volatile("s_waitcnt vmcnt(0)" ::: "memory");
;             const unsigned og = xb_add(&bar[XB_TOP], 1u);
;             const unsigned tg = og / nx;
;             if (og + 1u == (tg + 1u) * nx) xb_add(&bar[XB_TOPGEN], 1u);
;             else XB_SPIN(xb_ld(&bar[XB_TOPGEN]) == tg, bar);
;             __builtin_amdgcn_fence(__ATOMIC_ACQUIRE, "agent");
;             xb_add(&bar[XB_XGEN(b.x)], 1u);
.LBB0_169:
	s_or_b64 exec, exec, s[22:23]
	v_cvt_f32_u32_e32 v4, v2
	s_waitcnt vmcnt(0)
	v_readfirstlane_b32 s20, v3
	v_sub_u32_e32 v3, 0, v2
	v_rcp_iflag_f32_e32 v4, v4
	v_add_u32_e32 v5, s20, v1
	v_mul_f32_e32 v4, 0x4f7ffffe, v4
	v_cvt_u32_f32_e32 v4, v4
	v_mul_lo_u32 v1, v3, v4
	v_mul_hi_u32 v1, v4, v1
	v_add_u32_e32 v1, v4, v1
	v_mul_hi_u32 v1, v5, v1
	v_mul_lo_u32 v3, v1, v2
	v_sub_u32_e32 v3, v5, v3
	v_add_u32_e32 v4, 1, v1
	v_cmp_ge_u32_e32 vcc, v3, v2
	s_nop 1
	v_cndmask_b32_e32 v1, v1, v4, vcc
	v_sub_u32_e32 v4, v3, v2
	v_cndmask_b32_e32 v3, v3, v4, vcc
	v_add_u32_e32 v4, 1, v1
	v_cmp_ge_u32_e32 vcc, v3, v2
	v_add_u32_e32 v3, 1, v5
	s_nop 0
	v_cndmask_b32_e32 v1, v1, v4, vcc
	v_mul_lo_u32 v4, v2, v1
	v_add_u32_e32 v2, v4, v2
	s_waitcnt lgkmcnt(0)
	v_add_u32_e32 v4, 1, v1
	v_mul_lo_u32 v4, v4, v0
	v_mov_b32_e32 v5, 0x3000
	v_cmp_ne_u32_e32 vcc, v3, v2
	s_cbranch_vccnz .Lgb1_out
	buffer_wbl2 sc1
	s_waitcnt vmcnt(0) lgkmcnt(0)
	v_mov_b32_e32 v2, 1
	global_atomic_add v5, v2, s[26:27] offset:1024
.Lgb1_out:
	s_waitcnt vmcnt(0)

; #define LAS __attribute__((address_space(3)))
; #define TID() (wave * 64 + lane_id_v())
; __global__ void __launch_bounds__(512, 2) hymba_fwd(Args args) {
;     ...
;     if (IN(2)) {
;         LAS float* btab = (LAS float*)(lds + 8 * 12288);
;         const int tid = TID(), lane = tid & 63;
;         {
;             LAS float* rb = (LAS float*)(lds + 8 * 12288 + NH * 396 * 4);
;             LAS float* mhs = rb + 512;
;             LAS unsigned char* kbl = (LAS unsigned char*)(mhs + 16);
;             static_assert(8 * 12288 + NH * 396 * 4 + 2048 + 64 + 400 <= 131072, "P2 table scratch below the MoE tables");
;             rb[tid] = args.rel_bias[tid];
;             if (tid < 396) kbl[tid] = kBucket[tid / 132][tid % 132];
.LBB0_204:
	s_mov_b32 s98, 0
	s_add_u32 s8, s26, 0x8000000
	s_addc_u32 s9, s27, 0
	s_add_u32 s70, s26, 0x1d000000
	s_addc_u32 s71, s27, 0
	s_cmp_lt_i32 s94, 3
	s_cselect_b64 s[0:1], -1, 0
	s_cmp_gt_i32 s95, 2
	s_cselect_b64 s[20:21], -1, 0
	s_and_b64 s[0:1], s[0:1], s[20:21]
	s_andn2_b64 vcc, exec, s[0:1]
	s_cbranch_vccnz .LBB0_468
	s_waitcnt vmcnt(0)
	v_mbcnt_lo_u32_b32 v0, -1, 0
	v_mbcnt_hi_u32_b32 v0, -1, v0
	v_mov_b32_e32 v2, s6
	v_add_u32_e32 v156, s93, v0
	v_mov_b32_e32 v3, s7
	v_ashrrev_i32_e32 v157, 31, v156
	v_lshl_add_u64 v[2:3], v[156:157], 2, v[2:3]
	global_load_dword v3, v[2:3], off
	s_movk_i32 s0, 0x18c
	v_lshl_add_u32 v1, v156, 2, 0
	v_add_u32_e32 v2, 0x1e300, v1
	v_cmp_gt_i32_e32 vcc, s0, v156
	s_waitcnt vmcnt(0)
	ds_write_b32 v2, v3
	s_and_saveexec_b64 s[0:1], vcc
	s_cbranch_execz .LBB0_207
	s_mov_b32 s6, 0x3e0f83e1
	v_mul_hi_i32 v3, v156, s6
	v_lshrrev_b32_e32 v4, 31, v3
	v_ashrrev_i32_e32 v3, 5, v3
	s_getpc_b64 s[6:7]
	s_add_u32 s6, s6, kBucket@rel32@lo+4
	s_addc_u32 s7, s7, kBucket@rel32@hi+12
	v_add_u32_e32 v3, v3, v4
	s_movk_i32 s20, 0x84
	v_mov_b64_e32 v[4:5], s[6:7]
	v_mad_i64_i32 v[4:5], s[6:7], v3, s20, v[4:5]
	v_mul_lo_u32 v3, v3, s20
	v_sub_u32_e32 v6, v156, v3
	v_ashrrev_i32_e32 v7, 31, v6
	v_lshl_add_u64 v[4:5], v[4:5], 0, v[6:7]
	global_load_ubyte v3, v[4:5], off
	v_add_u32_e32 v4, 0, v156
	v_add_u32_e32 v4, 0x1eb40, v4
	s_waitcnt vmcnt(0)
	ds_write_b8 v4, v3

; #define LAS __attribute__((address_space(3)))
; __device__ __forceinline__ void attn_wave(const bf16* Q, const bf16* Kb, const bf16* Vb, bf16* MIX, int h, const int t0, LAS unsigned char* vbuf, const LAS float* bt, int lane) {
;     asm volatile("" : "+v"(lane));
;     const int qi = lane & 15, g = lane >> 4;
;     bf16x8 qf[2][2]; f32x4 o[2][4]; f32x4 lacc[2];
; #pragma unroll
;     for (int x = 0; x < 2; ++x) { const bf16* qrow = Q + (size_t)(t0 + 8 * x + 16 * qi) * AW + 64 * h + 8 * g; qf[x][0] = *(const bf16x8*)qrow; qf[x][1] = *(const bf16x8*)(qrow + 32);
;         lacc[x] = (f32x4){0.f, 0.f, 0.f, 0.f};
; #pragma unroll
;         for (int dt = 0; dt < 4; ++dt) o[x][dt] = (f32x4){0.f, 0.f, 0.f, 0.f}; }
;     const bf16* Kh = Kb + 64 * h; const bf16* Vh = Vb + 64 * h;
; __global__ void __launch_bounds__(512, 2) hymba_fwd(Args args) {
;     ...
;                 const bool doA = (((hs & 1) == 0) == (wave < 4));
;                 if (doA) { if (ia < nA) { const int a = bx + ia * G; const int blk = a >> 4, h = a & 15;
;                         attn_wave(Qb, Kb, Vb, MIX, h, 256 * blk + wave, vbuf, btab + h * 396, lane); ++ia; } }
.LBB0_214:
	s_and_b32 s0, s83, 1
	v_cmp_ne_u32_e32 vcc, s0, v223
	s_mov_b64 s[6:7], -1
	s_cbranch_vccnz .LBB0_234
	s_cmp_ge_i32 s82, s69
	s_mov_b32 s0, s82
	s_cbranch_scc1 .LBB0_233
	s_cmp_lg_u32 s98, 0
	s_cbranch_scc1 .Lp2gb_passed
	s_waitcnt vmcnt(0) lgkmcnt(0)
	v_mov_b32_e32 v21, 0x22604
	ds_read_b32 v233, v21
	v_mov_b32_e32 v21, 0x3000
	s_mov_b32 s99, 0
	s_waitcnt lgkmcnt(0)
	v_lshlrev_b32_e32 v233, 1, v233
.Lp2gb_spin:
	global_load_dword v22, v21, s[26:27] offset:1024 sc1
	s_waitcnt vmcnt(0)
	v_cmp_ge_u32_e32 vcc, v22, v233
	s_cbranch_vccnz .Lp2gb_done
	s_sleep 1
	s_add_i32 s99, s99, 1
	s_cmp_lt_u32 s99, 0x8000
	s_cbranch_scc1 .Lp2gb_spin
.Lp2gb_done:
	buffer_inv sc1
	s_waitcnt vmcnt(0)
	s_mov_b32 s98, 1
.Lp2gb_passed:
	s_mul_i32 s0, s82, s3
	s_add_i32 s0, s0, s2
	s_and_b32 s7, s0, 15
	s_lshl_b32 s0, s0, 4
	s_waitcnt vmcnt(14)
	v_mov_b32_e32 v22, v159
	s_and_b32 s0, s0, 0xffffff00
	s_add_i32 s6, s0, s92
	v_and_b32_e32 v233, 15, v22
	v_ashrrev_i32_e32 v21, 4, v22
	v_lshlrev_b32_e32 v224, 4, v233
	s_lshl_b32 s56, s7, 6
	s_lshl_b32 s21, s7, 7
	v_add_u32_e32 v174, s6, v224
	s_add_u32 s22, s38, s21
	v_lshlrev_b32_e32 v2, 3, v21
	s_addc_u32 s23, s39, 0
	v_ashrrev_i32_e32 v3, 31, v2
	v_ashrrev_i32_e32 v175, 31, v174
	v_lshl_add_u64 v[4:5], v[2:3], 1, s[22:23]
	v_lshlrev_b64 v[6:7], 11, v[174:175]
	v_lshl_add_u64 v[6:7], v[4:5], 0, v[6:7]
	global_load_dwordx4 v[12:15], v[6:7], off
	global_load_dwordx4 v[16:19], v[6:7], off offset:64
	v_add_u32_e32 v6, 8, v174
	v_ashrrev_i32_e32 v7, 31, v6
	v_lshlrev_b64 v[6:7], 11, v[6:7]
	v_lshl_add_u64 v[8:9], v[4:5], 0, v[6:7]
	global_load_dwordx4 v[4:7], v[8:9], off
	s_nop 0
	global_load_dwordx4 v[8:11], v[8:9], off offset:64
	v_lshlrev_b32_e32 v1, 1, v21
	v_bfe_u32 v3, v22, 3, 1
	v_lshlrev_b32_e32 v20, 5, v22
	v_lshlrev_b32_e32 v23, 3, v22
	v_and_or_b32 v1, v1, 2, v3
	v_lshlrev_b32_e32 v3, 9, v21
	v_and_b32_e32 v20, 0x180, v20
	v_and_b32_e32 v23, 24, v23
	v_or3_b32 v3, v20, v3, v23
	v_lshlrev_b32_e32 v1, 5, v1
	v_or_b32_e32 v24, v1, v3
	v_bitop3_b32 v25, v1, 32, v3 bitop3:0x36
	s_waitcnt vmcnt(17)
	v_bitop3_b32 v26, v1, 64, v3 bitop3:0x36
	v_bitop3_b32 v27, v1, s74, v3 bitop3:0x36
	v_and_b32_e32 v3, 7, v22
	v_lshrrev_b32_e32 v23, 3, v22
	v_lshlrev_b32_e32 v1, 3, v3
	v_bitop3_b32 v3, v23, v3, 6 bitop3:0x6c
	v_add_u32_e32 v29, 64, v22
	s_waitcnt vmcnt(16)
	v_add_u32_e32 v30, 0x80, v22
	v_add_u32_e32 v31, 0xc0, v22
	v_lshlrev_b32_e32 v23, 4, v3
	v_ashrrev_i32_e32 v3, 3, v22
	v_ashrrev_i32_e32 v173, 3, v29
	v_ashrrev_i32_e32 v188, 3, v30
	v_ashrrev_i32_e32 v189, 3, v31
	s_mul_i32 s0, s7, 0x630
	v_lshl_or_b32 v28, v3, 7, v23
	v_lshl_or_b32 v29, v173, 7, v23
	v_lshl_or_b32 v30, v188, 7, v23
	v_lshl_or_b32 v31, v189, 7, v23
	v_min_i32_e32 v23, 0x78, v174
	v_add_u32_e32 v191, 8, v23
	v_lshl_add_u32 v23, v233, 6, s0
	v_and_b32_e32 v22, -16, v22
	v_sub_u32_e32 v22, v23, v22
	s_ashr_i32 s7, s6, 31
	v_add_u32_e32 v193, s75, v22
	v_lshl_or_b32 v22, v189, 10, v1
	v_mov_b32_e32 v23, v171
	v_lshlrev_b64 v[176:177], 1, v[22:23]
	s_lshl_b64 s[22:23], s[6:7], 11
	v_lshl_or_b32 v22, v188, 10, v1
	v_lshl_add_u32 v170, v233, 10, v2
	s_or_b32 s21, s22, s21
	v_lshlrev_b64 v[178:179], 1, v[22:23]
	v_lshl_or_b32 v22, v173, 10, v1
	v_add_u32_e32 v20, 0x4000, v170
	v_lshlrev_b32_e32 v172, 2, v21
	v_mov_b32_e32 v21, v171
	s_add_u32 s44, s26, s21
	v_lshlrev_b64 v[180:181], 1, v[22:23]
	v_lshl_or_b32 v22, v3, 10, v1
	s_waitcnt vmcnt(15)
	v_mov_b32_e32 v36, 0
	v_min_i32_e32 v190, 0x80, v174
	v_sub_u32_e32 v192, v224, v172
	s_addc_u32 s45, s27, s23
	v_lshlrev_b64 v[182:183], 1, v[22:23]
	v_lshlrev_b64 v[184:185], 1, v[20:21]
	v_lshlrev_b64 v[186:187], 1, v[170:171]
	s_mov_b32 s57, 0
	v_add_u32_e32 v225, s68, v28
	v_add_u32_e32 v226, s68, v29
	v_add_u32_e32 v227, s68, v30
	v_add_u32_e32 v228, s68, v31
	v_add_u32_e32 v229, s68, v24
	v_add_u32_e32 v230, s68, v25
	v_add_u32_e32 v231, s68, v26
	v_add_u32_e32 v232, s68, v27
	v_mov_b32_e32 v37, v36
	s_waitcnt vmcnt(14)
	v_mov_b32_e32 v38, v36
	v_mov_b32_e32 v39, v36
	s_waitcnt vmcnt(11)
	v_mov_b32_e32 v56, v36
	v_mov_b32_e32 v57, v36
	s_waitcnt vmcnt(10)
	v_mov_b32_e32 v58, v36
	v_mov_b32_e32 v59, v36
	v_mov_b32_e32 v32, v36
	v_mov_b32_e32 v33, v36
	v_mov_b32_e32 v34, v36
	v_mov_b32_e32 v35, v36
	v_mov_b32_e32 v48, v36
	v_mov_b32_e32 v49, v36
	v_mov_b32_e32 v50, v36
	v_mov_b32_e32 v51, v36
	v_mov_b32_e32 v40, v36
	v_mov_b32_e32 v41, v36
	v_mov_b32_e32 v42, v36
	v_mov_b32_e32 v43, v36
	v_mov_b32_e32 v52, v36
	v_mov_b32_e32 v53, v36
	v_mov_b32_e32 v54, v36
	v_mov_b32_e32 v55, v36
	v_mov_b32_e32 v28, v36
	v_mov_b32_e32 v29, v36
	v_mov_b32_e32 v30, v36
	v_mov_b32_e32 v31, v36
	v_mov_b32_e32 v44, v36
	v_mov_b32_e32 v45, v36
	v_mov_b32_e32 v46, v36
	v_mov_b32_e32 v47, v36
	v_mov_b32_e32 v20, v36
	v_mov_b32_e32 v21, v36
	v_mov_b32_e32 v22, v36
	v_mov_b32_e32 v23, v36
	v_mov_b32_e32 v24, v36
	v_mov_b32_e32 v25, v36
	v_mov_b32_e32 v26, v36
	v_mov_b32_e32 v27, v36
